# v31 + RG-LRU pass-2 loop-top wait counts the previous chunk's two output stores (vmcnt(2)) instead of draining them
# baseline (speedup 1.0000x reference)
; #define LAS __attribute__((address_space(3)))
; template <bool FINAL> __device__ __forceinline__ void rglru_pass(Frame& F) {
;     ...
;     const float sp8 = -8.0f * 1.4426950408889634f * log1pf(__expf(-F.in[26][z * DM + ch]));
;     const int nch = FINAL ? 256 : NCHUNK;
;     LAS float* CWL = (LAS float*)(F.lds + 17408 + 32768 + 65536);
;     __syncthreads();
;     for (int i = F.tid; i < 640; i += 512) CWL[i] = i < 512 ? cw[(i >> 7) * DM + h * 128 + (i & 127)] : cb[h * 128 + (i - 512)];
;     __syncthreads();
;     LAS float* CL = (LAS float*)(F.lds + 17408 + 32768 + 65536 + 2560);
;     if (FINAL) { const int b = F.tid >> 8, zz = (F.tid >> 7) & 1, cl = F.tid & 127; const float* sb = SUM + ((size_t)zz * DM + h * 128 + cl) * 2;
;         float s = 0.f;
; #pragma unroll
;         for (int i = 0; i < 4; ++i) { const int c = 256 + b * 4 + (zz ? 3 - i : i); const float2 ab = *(const float2*)(sb + (size_t)c * 4 * DM); s = ab.x * s + ab.y; }
; #pragma unroll 8
;         for (int i = 0; i < 128; ++i) { const int c = b * 128 + (zz ? 127 - i : i); const float2 ab = *(const float2*)(sb + (size_t)c * 4 * DM);
;             const int d = c - cg; if (d >= 0 && d % ncg == 0) CL[(d / ncg) * 256 + zz * 128 + cl] = s;
;             s = ab.x * s + ab.y; }
;         __syncthreads(); }
;     v4u xq[2][4];
;     ...
;     if (cg < nch) RG_LOAD_ROWS(cg);
.LBB0_1583:
	s_or_b64 exec, exec, s[0:1]
	v_mul_f32_e32 v6, v17, v19
	v_mul_f32_e32 v6, v6, v20
	v_add_f32_e32 v7, v23, v6
	v_sub_f32_e32 v8, v7, v23
	v_sub_f32_e32 v6, v6, v8
	v_add_f32_e32 v6, v22, v6
	v_add_f32_e32 v8, v7, v6
	v_add_f32_e32 v4, v16, v21
	v_sub_f32_e32 v7, v8, v7
	v_sub_f32_e32 v6, v6, v7
	v_add_f32_e32 v7, v4, v8
	v_sub_f32_e32 v9, v7, v4
	v_sub_f32_e32 v5, v4, v16
	v_sub_f32_e32 v10, v7, v9
	v_sub_f32_e32 v5, v21, v5
	v_sub_f32_e32 v4, v4, v10
	v_sub_f32_e32 v8, v8, v9
	v_add_f32_e32 v4, v8, v4
	v_add_f32_e32 v8, v5, v6
	v_sub_f32_e32 v9, v8, v5
	v_sub_f32_e32 v10, v8, v9
	v_sub_f32_e32 v5, v5, v10
	v_sub_f32_e32 v6, v6, v9
	v_add_f32_e32 v4, v8, v4
	v_add_f32_e32 v5, v6, v5
	v_add_f32_e32 v6, v7, v4
	v_sub_f32_e32 v7, v6, v7
	v_sub_f32_e32 v4, v4, v7
	v_add_f32_e32 v4, v5, v4
	s_mov_b32 s0, 0x7f800000
	v_add_f32_e32 v4, v6, v4
	v_mov_b32_e32 v5, 0x7f800000
	v_cmp_neq_f32_e32 vcc, s0, v15
	s_mov_b32 s0, 0x33800000
	v_lshlrev_b32_e32 v3, 2, v3
	v_cndmask_b32_e32 v4, v5, v4, vcc
	v_mov_b32_e32 v5, 0x7fc00000
	v_cmp_ngt_f32_e32 vcc, -1.0, v15
	v_lshlrev_b32_e32 v40, 11, v14
	v_add_u32_e32 v42, 0, v3
	v_cndmask_b32_e32 v4, v5, v4, vcc
	v_mov_b32_e32 v5, 0xff800000
	v_cmp_neq_f32_e32 vcc, -1.0, v15
	v_mul_f32_e32 v35, 0x4f7ffffe, v35
	s_movk_i32 s5, 0x110
	v_cndmask_b32_e32 v4, v5, v4, vcc
	v_cmp_gt_f32_e32 vcc, s0, v1
	s_lshl_b32 s0, s23, 1
	s_add_u32 s16, s6, s0
	s_addc_u32 s17, s7, 0
	s_lshl_b32 s0, s22, 9
	v_add_u32_e32 v175, v42, v40
	v_or_b32_e32 v43, 0x4000, v40
	v_or_b32_e32 v44, 0x5000, v40
	v_or_b32_e32 v45, 0x6000, v40
	v_or_b32_e32 v46, 0x7000, v40
	v_lshl_add_u64 v[40:41], s[88:89], 0, v[172:173]
	s_mov_b64 s[22:23], 0x21c00000
	v_cvt_u32_f32_e32 v35, v35
	v_lshl_add_u64 v[184:185], v[40:41], 0, s[22:23]
	v_mul_lo_u32 v41, v36, s5
	v_add_u32_e32 v194, 0, v41
	v_mul_lo_u32 v41, v38, s5
	s_movk_i32 s5, 0xf0
	s_add_i32 s0, s0, 0
	v_lshlrev_b32_e32 v47, 2, v37
	v_lshlrev_b32_e32 v186, 1, v37
	v_add_u32_e32 v195, 0, v41
	v_mov_b32_e32 v187, v173
	v_mul_lo_u32 v41, v36, s5
	s_add_i32 s0, s0, 0x1ce00
	v_lshl_add_u64 v[188:189], s[16:17], 0, v[186:187]
	v_add3_u32 v187, v194, v41, v47
	v_mul_lo_u32 v41, v38, s5
	v_readfirstlane_b32 s5, v35
	s_cmpk_gt_u32 s95, 0xff
	s_mul_i32 s4, s4, s5
	v_cndmask_b32_e32 v1, v4, v15, vcc
	s_cselect_b64 s[8:9], -1, 0
	s_add_i32 s12, 0, 0x1cc00
	s_mul_hi_u32 s4, s5, s4
	s_add_i32 s17, s20, s21
	v_mul_f32_e32 v182, 0xc138aa3b, v1
	v_lshl_add_u32 v39, v14, 4, 0
	v_mul_u32_u24_e32 v34, 0x110, v34
	v_add_u32_e32 v48, 0, v47
	v_add_u32_e32 v179, s12, v47
	s_add_i32 s12, 0, 0x1c400
	v_lshlrev_b32_e32 v40, 9, v36
	v_lshlrev_b32_e32 v37, 9, v38
	v_add3_u32 v197, v195, v41, v47
	s_add_i32 s16, s5, s4
	s_lshl_b32 s4, s17, 6
	s_lshl_b32 s18, s21, 6
	v_mbcnt_lo_u32_b32 v35, -1, 0
	s_mov_b32 s15, 0
	v_add_u32_e32 v1, s0, v3
	v_mov_b32_e32 v183, v182
	v_cmp_ne_u32_e64 s[0:1], 0, v14
	v_mov_b32_e32 v3, v2
	v_mov_b32_e32 v4, v2
	v_mov_b32_e32 v5, v2
	v_mov_b32_e32 v6, v2
	v_mov_b32_e32 v7, v2
	v_mov_b32_e32 v8, v2
	v_mov_b32_e32 v9, v2
	v_mov_b32_e32 v10, v2
	v_mov_b32_e32 v11, v2
	v_mov_b32_e32 v12, v2
	v_mov_b32_e32 v13, v2
	v_mov_b32_e32 v14, v2
	v_mov_b32_e32 v15, v2
	v_mov_b32_e32 v16, v2
	v_mov_b32_e32 v17, v2
	v_mov_b32_e32 v19, v18
	v_mov_b32_e32 v20, v18
	v_mov_b32_e32 v21, v18
	v_mov_b32_e32 v22, v18
	v_mov_b32_e32 v23, v18
	v_mov_b32_e32 v24, v18
	v_mov_b32_e32 v25, v18
	v_mov_b32_e32 v26, v18
	v_mov_b32_e32 v27, v18
	v_mov_b32_e32 v28, v18
	v_mov_b32_e32 v29, v18
	v_mov_b32_e32 v30, v18
	v_mov_b32_e32 v31, v18
	v_mov_b32_e32 v32, v18
	v_mov_b32_e32 v33, v18
	v_add_u32_e32 v177, 0xc400, v175
	v_cmp_gt_u32_e64 s[2:3], 32, v178
	v_add_u32_e32 v181, s12, v47
	v_add_u32_e32 v196, 0xc400, v187
	v_add_u32_e32 v198, 0xc400, v197
	v_add_u32_e32 v199, s4, v38
	v_add_u32_e32 v200, s4, v36
	s_add_i32 s19, s19, s18
	v_add_u32_e32 v201, v48, v40
	v_add_u32_e32 v202, v48, v37
	v_mbcnt_hi_u32_b32 v203, -1, v35
	s_mov_b32 s12, 0xbfb8aa3b
	v_add_u32_e32 v204, v42, v43
	v_add_u32_e32 v205, v42, v44
	v_add_u32_e32 v206, v42, v45
	v_add_u32_e32 v207, v42, v46
	v_mov_b32_e32 v158, 0
	v_add_u32_e32 v208, v39, v34
	s_mov_b32 s22, 0
	s_waitcnt vmcnt(0)
	s_branch .LBB0_1585

; #define LAS __attribute__((address_space(3)))
; #define LDS_BARRIER() do { asm volatile("s_waitcnt lgkmcnt(0)" ::: "memory"); __builtin_amdgcn_s_barrier(); asm volatile("" ::: "memory"); } while (0)
; __device__ __forceinline__ unsigned pk2(float lo, float hi) { return pg8::cvt_pk_bf16(lo, hi); }
; template <bool FINAL> __device__ __forceinline__ void rglru_pass(Frame& F) {
;     ...
;     for (int c = cg; c < nch; c += ncg) {
;         const int row0 = c < 256 ? c * 64 : ML + (c - 256) * 64;
;         LDS_BARRIER();
; #pragma unroll
;         for (int it = 0; it < 2; ++it) { const int id = F.tid + 512 * it, t = id >> 4, c8 = (id & 15) * 8;
;             float a[8];
;             { const f32x4 b0 = *(const LAS f32x4*)(CWL + 512 + c8), b1 = *(const LAS f32x4*)(CWL + 512 + c8 + 4);
;               a[0] = b0.x; a[1] = b0.y; a[2] = b0.z; a[3] = b0.w; a[4] = b1.x; a[5] = b1.y; a[6] = b1.z; a[7] = b1.w; }
; #pragma unroll
;             for (int tap = 0; tap < 4; ++tap) { const v4u x = xq[it][tap];
;                 const f32x4 w0 = *(const LAS f32x4*)(CWL + tap * 128 + c8), w1 = *(const LAS f32x4*)(CWL + tap * 128 + c8 + 4);
;                 a[0] += w0.x * bflo(x[0]); a[1] += w0.y * bfhi(x[0]); a[2] += w0.z * bflo(x[1]); a[3] += w0.w * bfhi(x[1]);
;                 a[4] += w1.x * bflo(x[2]); a[5] += w1.y * bfhi(x[2]); a[6] += w1.z * bflo(x[3]); a[7] += w1.w * bfhi(x[3]); }
;             *(LAS f32x4*)(XCF + t * 128 + c8) = (f32x4){a[0], a[1], a[2], a[3]}; *(LAS f32x4*)(XCF + t * 128 + c8 + 4) = (f32x4){a[4], a[5], a[6], a[7]};
;             v4u w; w.x = pk2(a[0], a[1]); w.y = pk2(a[2], a[3]); w.z = pk2(a[4], a[5]); w.w = pk2(a[6], a[7]);
;             *(LAS v4u*)(XCB + t * 272 + c8 * 2) = w; }
;         LDS_BARRIER();
;         if (c + ncg < nch) RG_LOAD_ROWS(c + ncg);
.LBB0_1585:
	s_waitcnt lgkmcnt(0)
	s_barrier
	ds_read_b128 v[34:37], v179
	ds_read_b128 v[38:41], v179 offset:16
	ds_read_b128 v[42:45], v181
	ds_read_b128 v[46:49], v181 offset:16
	ds_read_b128 v[50:53], v181 offset:512
	ds_read_b128 v[54:57], v181 offset:528
	ds_read_b128 v[58:61], v181 offset:1024
	ds_read_b128 v[62:65], v181 offset:1040
	ds_read_b128 v[164:167], v181 offset:1536
	ds_read_b128 v[168:171], v181 offset:1552
	s_waitcnt vmcnt(2)
	v_lshlrev_b32_e32 v190, 16, v134
	v_and_b32_e32 v191, 0xffff0000, v134
	s_waitcnt lgkmcnt(7)
	v_pk_fma_f32 v[34:35], v[42:43], v[190:191], v[34:35]
	v_lshlrev_b32_e32 v42, 16, v130
	v_and_b32_e32 v43, 0xffff0000, v130
	s_waitcnt lgkmcnt(5)
	v_pk_fma_f32 v[34:35], v[50:51], v[42:43], v[34:35]
	v_lshlrev_b32_e32 v42, 16, v138
	v_and_b32_e32 v43, 0xffff0000, v138
	s_waitcnt lgkmcnt(3)
	v_pk_fma_f32 v[34:35], v[58:59], v[42:43], v[34:35]
	v_lshlrev_b32_e32 v42, 16, v142
	v_and_b32_e32 v43, 0xffff0000, v142
	s_waitcnt lgkmcnt(1)
	v_pk_fma_f32 v[34:35], v[164:165], v[42:43], v[34:35]
	v_lshlrev_b32_e32 v42, 16, v135
	v_and_b32_e32 v43, 0xffff0000, v135
	v_pk_fma_f32 v[36:37], v[44:45], v[42:43], v[36:37]
	v_lshlrev_b32_e32 v42, 16, v131
	v_and_b32_e32 v43, 0xffff0000, v131
	v_pk_fma_f32 v[36:37], v[52:53], v[42:43], v[36:37]
	v_lshlrev_b32_e32 v42, 16, v139
	v_and_b32_e32 v43, 0xffff0000, v139
	v_pk_fma_f32 v[36:37], v[60:61], v[42:43], v[36:37]
	v_lshlrev_b32_e32 v42, 16, v143
	v_and_b32_e32 v43, 0xffff0000, v143
	v_pk_fma_f32 v[36:37], v[166:167], v[42:43], v[36:37]
	v_lshlrev_b32_e32 v42, 16, v136
	v_and_b32_e32 v43, 0xffff0000, v136
	v_pk_fma_f32 v[38:39], v[46:47], v[42:43], v[38:39]
	v_lshlrev_b32_e32 v42, 16, v132
	v_and_b32_e32 v43, 0xffff0000, v132
	v_pk_fma_f32 v[38:39], v[54:55], v[42:43], v[38:39]
	v_lshlrev_b32_e32 v42, 16, v140
	v_and_b32_e32 v43, 0xffff0000, v140
	v_pk_fma_f32 v[38:39], v[62:63], v[42:43], v[38:39]
	v_lshlrev_b32_e32 v42, 16, v144
	v_and_b32_e32 v43, 0xffff0000, v144
	s_waitcnt lgkmcnt(0)
	v_pk_fma_f32 v[38:39], v[168:169], v[42:43], v[38:39]
	v_lshlrev_b32_e32 v42, 16, v137
	v_and_b32_e32 v43, 0xffff0000, v137
	v_pk_fma_f32 v[40:41], v[48:49], v[42:43], v[40:41]
	v_lshlrev_b32_e32 v42, 16, v133
	v_and_b32_e32 v43, 0xffff0000, v133
	v_pk_fma_f32 v[40:41], v[56:57], v[42:43], v[40:41]
	v_lshlrev_b32_e32 v42, 16, v141
	v_and_b32_e32 v43, 0xffff0000, v141
	v_pk_fma_f32 v[40:41], v[64:65], v[42:43], v[40:41]
	v_lshlrev_b32_e32 v42, 16, v145
	v_and_b32_e32 v43, 0xffff0000, v145
	v_pk_fma_f32 v[40:41], v[170:171], v[42:43], v[40:41]
	ds_write_b128 v201, v[34:37] offset:17408
	ds_write_b128 v201, v[38:41] offset:17424
	v_cvt_pk_bf16_f32 v34, v34, v35
	v_cvt_pk_bf16_f32 v35, v36, v37
	v_cvt_pk_bf16_f32 v36, v38, v39
	v_add_u32_e32 v38, v194, v186
	v_cvt_pk_bf16_f32 v37, v40, v41
	ds_write_b128 v38, v[34:37]
	ds_read_b128 v[34:37], v179
	ds_read_b128 v[38:41], v179 offset:16
	ds_read_b128 v[42:45], v181
	ds_read_b128 v[46:49], v181 offset:16
	ds_read_b128 v[50:53], v181 offset:512
	ds_read_b128 v[54:57], v181 offset:528
	ds_read_b128 v[58:61], v181 offset:1024
	ds_read_b128 v[62:65], v181 offset:1040
	ds_read_b128 v[164:167], v181 offset:1536
	ds_read_b128 v[168:171], v181 offset:1552
	v_lshlrev_b32_e32 v190, 16, v146
	v_and_b32_e32 v191, 0xffff0000, v146
	s_waitcnt lgkmcnt(7)
	v_pk_fma_f32 v[34:35], v[42:43], v[190:191], v[34:35]
	v_lshlrev_b32_e32 v42, 16, v150
	v_and_b32_e32 v43, 0xffff0000, v150
	s_waitcnt lgkmcnt(5)
	v_pk_fma_f32 v[34:35], v[50:51], v[42:43], v[34:35]
	v_lshlrev_b32_e32 v42, 16, v154
	v_and_b32_e32 v43, 0xffff0000, v154
	s_waitcnt lgkmcnt(3)
	v_pk_fma_f32 v[34:35], v[58:59], v[42:43], v[34:35]
	v_lshlrev_b32_e32 v42, 16, v160
	v_and_b32_e32 v43, 0xffff0000, v160
	s_waitcnt lgkmcnt(1)
	v_pk_fma_f32 v[34:35], v[164:165], v[42:43], v[34:35]
	v_lshlrev_b32_e32 v42, 16, v147
	v_and_b32_e32 v43, 0xffff0000, v147
	v_pk_fma_f32 v[36:37], v[44:45], v[42:43], v[36:37]
	v_lshlrev_b32_e32 v42, 16, v151
	v_and_b32_e32 v43, 0xffff0000, v151
	v_pk_fma_f32 v[36:37], v[52:53], v[42:43], v[36:37]
	v_lshlrev_b32_e32 v42, 16, v155
	v_and_b32_e32 v43, 0xffff0000, v155
	v_pk_fma_f32 v[36:37], v[60:61], v[42:43], v[36:37]
	v_lshlrev_b32_e32 v42, 16, v161
	v_and_b32_e32 v43, 0xffff0000, v161
	v_pk_fma_f32 v[36:37], v[166:167], v[42:43], v[36:37]
	v_lshlrev_b32_e32 v42, 16, v148
	v_and_b32_e32 v43, 0xffff0000, v148
	v_pk_fma_f32 v[38:39], v[46:47], v[42:43], v[38:39]
	v_lshlrev_b32_e32 v42, 16, v152
	v_and_b32_e32 v43, 0xffff0000, v152
	v_pk_fma_f32 v[38:39], v[54:55], v[42:43], v[38:39]
	v_lshlrev_b32_e32 v42, 16, v156
	v_and_b32_e32 v43, 0xffff0000, v156
	v_pk_fma_f32 v[38:39], v[62:63], v[42:43], v[38:39]
	v_lshlrev_b32_e32 v42, 16, v162
	v_and_b32_e32 v43, 0xffff0000, v162
	s_waitcnt lgkmcnt(0)
	v_pk_fma_f32 v[38:39], v[168:169], v[42:43], v[38:39]
	v_lshlrev_b32_e32 v42, 16, v149
	v_and_b32_e32 v43, 0xffff0000, v149
	v_pk_fma_f32 v[40:41], v[48:49], v[42:43], v[40:41]
	v_lshlrev_b32_e32 v42, 16, v153
	v_and_b32_e32 v43, 0xffff0000, v153
	v_pk_fma_f32 v[40:41], v[56:57], v[42:43], v[40:41]
	v_lshlrev_b32_e32 v42, 16, v157
	v_and_b32_e32 v43, 0xffff0000, v157
	v_pk_fma_f32 v[40:41], v[64:65], v[42:43], v[40:41]
	v_lshlrev_b32_e32 v42, 16, v163
	v_and_b32_e32 v43, 0xffff0000, v163
	v_pk_fma_f32 v[40:41], v[170:171], v[42:43], v[40:41]
	ds_write_b128 v202, v[34:37] offset:17408
	ds_write_b128 v202, v[38:41] offset:17424
	v_cvt_pk_bf16_f32 v34, v34, v35
	v_cvt_pk_bf16_f32 v35, v36, v37
	v_cvt_pk_bf16_f32 v36, v38, v39
	v_add_u32_e32 v38, v195, v186
	v_cvt_pk_bf16_f32 v37, v40, v41
	ds_write_b128 v38, v[34:37]
	s_waitcnt lgkmcnt(0)
	s_barrier
	s_add_i32 s4, s17, s22
	s_cmpk_gt_i32 s4, 0xff
	s_cbranch_scc1 .LBB0_1603
	s_add_i32 s4, s19, s15
	s_and_b32 s23, s4, 0xffffe000
	s_mov_b32 s76, s23
	s_mov_b32 s77, 0
	s_lshl_b64 s[76:77], s[76:77], 13
	s_add_u32 s76, s76, 0x1000
	s_addc_u32 s77, s77, 0
	s_add_u32 s68, s6, s76
	s_addc_u32 s69, s7, s77
	s_and_b32 s69, s69, 0xffff
	s_mov_b32 s70, 0x3fff000
	s_mov_b32 s71, 0x20000
	s_sub_i32 s78, s15, s23
	s_add_i32 s78, s78, -2
	v_add_u32_e32 v34, s78, v200
	v_lshl_add_u32 v34, v34, 13, v172
	buffer_load_dwordx4 v[134:137], v34, s[68:71], 0 offen
	v_add_u32_e32 v35, 0x2000, v34
	buffer_load_dwordx4 v[130:133], v35, s[68:71], 0 offen
	v_add_u32_e32 v36, 0x4000, v34
	buffer_load_dwordx4 v[138:141], v36, s[68:71], 0 offen
	v_add_u32_e32 v37, 0x6000, v34
	buffer_load_dwordx4 v[142:145], v37, s[68:71], 0 offen
	v_add_u32_e32 v34, s78, v199
	v_lshl_add_u32 v34, v34, 13, v172
	buffer_load_dwordx4 v[146:149], v34, s[68:71], 0 offen
	v_add_u32_e32 v35, 0x2000, v34
	buffer_load_dwordx4 v[150:153], v35, s[68:71], 0 offen
	v_add_u32_e32 v36, 0x4000, v34
	buffer_load_dwordx4 v[154:157], v36, s[68:71], 0 offen
	v_add_u32_e32 v37, 0x6000, v34
	buffer_load_dwordx4 v[160:163], v37, s[68:71], 0 offen
	v_mov_b32_e32 v159, v158
